# speedup vs baseline: 1.0047x; 1.0047x over previous
.Lskip_tabld:
	v_readfirstlane_b32 s4, v156
	s_ashr_i32 s27, s4, 7
	s_lshl_b32 s0, s27, 1
	s_ashr_i32 s1, s0, 31
	s_lshl_b64 s[2:3], s[0:1], 13
	s_add_u32 s2, s8, s2
	s_addc_u32 s3, s9, s3
	s_add_u32 s28, s2, 0x18000
	s_addc_u32 s29, s3, 0
	v_lshlrev_b32_e32 v154, 4, v167
	v_lshl_add_u64 v[6:7], s[28:29], 0, v[154:155]
	v_or_b32_e32 v8, 0x800, v169
	v_add_co_u32_e32 v6, vcc, s23, v6
	v_lshlrev_b32_e32 v168, 1, v8
	s_nop 0
	v_addc_co_u32_e32 v7, vcc, 0, v7, vcc
	global_load_dwordx4 v[150:153], v154, s[28:29]
	global_load_dwordx4 v[146:149], v154, s[28:29] offset:1024
	global_load_dwordx4 v[142:145], v154, s[28:29] offset:2048
	global_load_dwordx4 v[138:141], v154, s[28:29] offset:3072
	global_load_dwordx4 v[126:129], v[6:7], off offset:1024
	global_load_dwordx4 v[122:125], v[6:7], off offset:2048
	global_load_dwordx4 v[134:137], v168, s[28:29]
	global_load_dwordx4 v[130:133], v[6:7], off offset:3072
	v_lshl_add_u64 v[6:7], s[2:3], 0, v[154:155]
	v_lshl_add_u64 v[8:9], v[6:7], 0, s[16:17]
	v_add_co_u32_e32 v6, vcc, 0x28000, v6
	s_nop 1
	v_addc_co_u32_e32 v7, vcc, 0, v7, vcc
	global_load_dwordx4 v[86:89], v[6:7], off
	global_load_dwordx4 v[82:85], v[8:9], off offset:1024
	v_lshrrev_b32_e32 v182, 5, v167
	s_ashr_i32 s2, s4, 6
	s_lshl_b32 s3, s2, 3
	s_and_b32 s5, s3, 8
	s_bfe_u32 s26, s2, 0x10001
	s_or_b32 s5, s26, s5
	s_lshl_b32 s26, s2, 9
	s_and_b32 s26, s26, 0x400
	s_lshl_b32 s5, s5, 4
	s_or_b32 s28, s5, s26
	v_bfe_u32 v76, v156, 4, 1
	v_bitop3_b32 v77, v182, v156, 1 bitop3:0x78
	v_lshlrev_b32_e32 v154, 2, v182
	v_xor_b32_e32 v77, v77, v76
	v_bitop3_b32 v78, v154, v156, 4 bitop3:0x78
	v_and_b32_e32 v79, 10, v156
	v_or3_b32 v77, v79, v78, v77
	s_lshl_b32 s5, s2, 4
	v_lshlrev_b32_e32 v77, 4, v77
	s_lshl_b32 s3, s2, 13
	s_and_b32 s29, s5, 16
	v_lshlrev_b32_e32 v170, 8, v182
	v_lshl_or_b32 v171, v76, 10, v77
	s_or_b32 s26, s29, s3
	v_bitop3_b32 v179, v171, s26, v170 bitop3:0x36
	s_or_b32 s5, s26, 0x280
	v_bitop3_b32 v178, v171, s5, v170 bitop3:0x36
	s_or_b32 s30, s3, 0x800
	s_or_b32 s33, s3, 0x1000
	s_or_b32 s29, s29, 64
	s_or_b32 s34, s29, s33
	v_bitop3_b32 v180, v171, s34, v170 bitop3:0x36
	s_or_b32 s29, s3, s29
	s_or_b32 s29, s29, 0x1280
	s_and_b32 s5, s2, 1
	s_lshl_b32 s31, s5, 4
	s_or_b32 s2, s31, s3
	v_bitop3_b32 v173, v171, s2, v170 bitop3:0x36
	v_bitop3_b32 v76, v156, 31, v156 bitop3:0xc
	v_lshrrev_b32_e32 v77, 4, v76
	v_bitop3_b32 v78, v76, v182, 1 bitop3:0x6c
	v_xor_b32_e32 v78, v78, v77
	v_bitop3_b32 v76, v76, v154, 4 bitop3:0x6c
	v_bitop3_b32 v79, v156, 10, 31 bitop3:8
	v_or3_b32 v76, v79, v76, v78
	v_lshlrev_b32_e32 v77, 10, v77
	v_lshlrev_b32_e32 v76, 4, v76
	v_or3_b32 v154, v77, v76, v170
	v_bitop3_b32 v172, s2, v154, v159 bitop3:0x36
	v_bitop3_b32 v176, v171, s29, v170 bitop3:0x36
	s_or_b32 s29, s31, s30
	s_or_b32 s29, s29, 0xa0
	v_bitop3_b32 v175, v171, s29, v170 bitop3:0x36
	s_or_b32 s29, s2, 0xaa0
	s_xor_b32 s29, s29, 0x80
	v_xor_b32_e32 v174, s29, v154
	s_or_b32 s29, s26, 0x18e0
	v_bitop3_b32 v181, v171, s29, v170 bitop3:0x36
	s_or_b32 s29, s26, 0x1a60
	v_bitop3_b32 v177, v171, s29, v170 bitop3:0x36
	s_or_b32 s29, s31, 64
	s_or_b32 s3, s3, s29
	s_mov_b32 s41, s3
	s_or_b32 s29, s29, s33
	s_mov_b32 s40, s29
	s_or_b32 s3, s2, 0x18e0
	s_mov_b32 s42, s3
	s_or_b32 s2, s2, 0x1ae0
	s_xor_b32 s2, s2, 0x80
	s_mov_b32 s43, s2
	v_lshl_add_u32 v166, v156, 2, v165
	s_cmp_lt_i32 s22, 0
	s_cbranch_scc0 .Lskip_stage0
	v_lshl_add_u32 v6, v156, 3, v1
	v_cmp_gt_i32_e32 vcc, 64, v156
	s_waitcnt vmcnt(11)
	ds_write_b64 v6, v[4:5]
	s_and_saveexec_b64 s[2:3], vcc
	s_cbranch_execz .LBB1_7
	s_waitcnt vmcnt(10)
	ds_write_b64 v6, v[2:3] offset:2048

.Lskip_stage0:
	s_lshr_b32 s38, s4, 1
	v_and_b32_e32 v26, 31, v167
	v_and_b32_e32 v27, 3, v167
	v_bfe_u32 v28, v167, 3, 1
	v_bfe_u32 v29, v167, 2, 1
	v_lshl_or_b32 v27, v28, 2, v27
	v_lshl_or_b32 v27, v29, 3, v27
	v_lshlrev_b32_e32 v32, 9, v182
	v_lshl_add_u32 v30, v27, 3, v32
	v_add_u32_e32 v30, 0x10000, v30
	v_lshl_add_u32 v31, v26, 3, v32
	v_add_u32_e32 v31, 0x10400, v31
	v_xor_b32_e32 v28, 31, v26
	v_lshl_add_u32 v28, v28, 3, v32
	v_add_u32_e32 v28, 0x10400, v28
	v_bfe_u32 v29, v167, 4, 1
	v_mul_u32_u24_e32 v29, 0x78, v29
	v_xor_b32_e32 v254, s38, v29
	v_or_b32_e32 v254, 0x10800, v254
	v_and_b32_e32 v33, 16, v167
	v_cmp_eq_u32_e32 vcc, 0, v33
	ds_read2_b64 v[66:69], v30 offset0:0 offset1:32
	ds_read2_b64 v[70:73], v30 offset0:16 offset1:48
	ds_read2_b64 v[198:201], v31 offset0:0 offset1:32
	ds_read2_b64 v[202:205], v28 offset0:0 offset1:32
	ds_read2_b64 v[206:209], v254 offset0:0 offset1:16
	ds_read2_b64 v[210:213], v254 offset0:32 offset1:48
	s_waitcnt lgkmcnt(0)
	v_cndmask_b32_e32 v74, v67, v66, vcc
	v_cndmask_b32_e32 v75, v69, v68, vcc
	v_cndmask_b32_e64 v76, v66, -v67, vcc
	v_cndmask_b32_e64 v77, v68, -v69, vcc
	v_cndmask_b32_e32 v78, v71, v70, vcc
	v_cndmask_b32_e32 v79, v73, v72, vcc
	v_cndmask_b32_e64 v80, v70, -v71, vcc
	v_cndmask_b32_e64 v81, v72, -v73, vcc
	v_cvt_pk_f16_f32 v190, v74, v75
	v_cvt_pk_f16_f32 v191, v74, v75
	v_cvt_pk_f16_f32 v192, v76, v77
	v_cvt_pk_f16_f32 v193, v76, v77
	v_cvt_pk_f16_f32 v194, v78, v79
	v_cvt_pk_f16_f32 v195, v78, v79
	v_cvt_pk_f16_f32 v196, v80, v81
	v_cvt_pk_f16_f32 v197, v80, v81
	v_mul_f32_e32 v66, v199, v207
	v_mul_f32_e32 v68, v199, v206
	v_mul_f32_e32 v67, v199, v209
	v_mul_f32_e32 v69, v199, v208
	v_fma_f32 v66, v198, v206, -v66
	v_fma_f32 v68, v198, v207, v68
	v_fma_f32 v67, v198, v208, -v67
	v_fma_f32 v69, v198, v209, v69
	v_cvt_pk_f16_f32 v214, v66, v67
	v_cvt_pk_f16_f32 v216, v68, v69
	v_mul_f32_e32 v70, v201, v211
	v_mul_f32_e32 v72, v201, v210
	v_mul_f32_e32 v71, v201, v213
	v_mul_f32_e32 v73, v201, v212
	v_fma_f32 v70, v200, v210, -v70
	v_fma_f32 v72, v200, v211, v72
	v_fma_f32 v71, v200, v212, -v71
	v_fma_f32 v73, v200, v213, v73
	v_cvt_pk_f16_f32 v215, v70, v71
	v_cvt_pk_f16_f32 v217, v72, v73
	v_mul_f32_e32 v66, v203, v207
	v_mul_f32_e32 v68, v203, v206
	v_mul_f32_e32 v67, v203, v209
	v_mul_f32_e32 v69, v203, v208
	v_fma_f32 v66, v202, v206, -v66
	v_fma_f32 v68, v202, v207, v68
	v_fma_f32 v67, v202, v208, -v67
	v_fma_f32 v69, v202, v209, v69
	v_cvt_pk_f16_f32 v218, v66, v67
	v_cvt_pk_f16_f32 v220, v68, v69
	v_mul_f32_e32 v70, v205, v211
	v_mul_f32_e32 v72, v205, v210
	v_mul_f32_e32 v71, v205, v213
	v_mul_f32_e32 v73, v205, v212
	v_fma_f32 v70, v204, v210, -v70
	v_fma_f32 v72, v204, v211, v72
	v_fma_f32 v71, v204, v212, -v71
	v_fma_f32 v73, v204, v213, v73
	v_cvt_pk_f16_f32 v219, v70, v71
	v_cvt_pk_f16_f32 v221, v72, v73
	v_xor_b32_e32 v255, 8, v254
	ds_read2_b64 v[206:209], v255 offset0:0 offset1:16
	ds_read2_b64 v[210:213], v255 offset0:32 offset1:48
	v_mfma_f32_32x32x16_f16 v[2:17], v[190:193], v[214:217], 0
	v_mfma_f32_32x32x16_f16 v[18:33], v[194:197], v[218:221], 0
	s_waitcnt lgkmcnt(0)
	v_mul_f32_e32 v66, v199, v207
	v_mul_f32_e32 v68, v199, v206
	v_mul_f32_e32 v67, v199, v209
	v_mul_f32_e32 v69, v199, v208
	v_fma_f32 v66, v198, v206, -v66
	v_fma_f32 v68, v198, v207, v68
	v_fma_f32 v67, v198, v208, -v67
	v_fma_f32 v69, v198, v209, v69
	v_cvt_pk_f16_f32 v214, v66, v67
	v_cvt_pk_f16_f32 v216, v68, v69
	v_mul_f32_e32 v70, v201, v211
	v_mul_f32_e32 v72, v201, v210
	v_mul_f32_e32 v71, v201, v213
	v_mul_f32_e32 v73, v201, v212
	v_fma_f32 v70, v200, v210, -v70
	v_fma_f32 v72, v200, v211, v72
	v_fma_f32 v71, v200, v212, -v71
	v_fma_f32 v73, v200, v213, v73
	v_cvt_pk_f16_f32 v215, v70, v71
	v_cvt_pk_f16_f32 v217, v72, v73
	v_cvt_pk_f16_f32 v2, v2, v3
	v_cvt_pk_f16_f32 v3, v4, v5
	v_cvt_pk_f16_f32 v4, v6, v7
	v_cvt_pk_f16_f32 v5, v8, v9
	v_cvt_pk_f16_f32 v6, v10, v11
	v_cvt_pk_f16_f32 v7, v12, v13
	v_cvt_pk_f16_f32 v8, v14, v15
	v_cvt_pk_f16_f32 v9, v16, v17
	v_cvt_pk_f16_f32 v18, v18, v19
	v_cvt_pk_f16_f32 v19, v20, v21
	v_cvt_pk_f16_f32 v20, v22, v23
	v_cvt_pk_f16_f32 v21, v24, v25
	v_cvt_pk_f16_f32 v22, v26, v27
	v_cvt_pk_f16_f32 v23, v28, v29
	v_cvt_pk_f16_f32 v24, v30, v31
	v_cvt_pk_f16_f32 v25, v32, v33
	s_setprio 1
	s_waitcnt vmcnt(6)
	v_mul_f32_e32 v66, v203, v207
	v_mul_f32_e32 v68, v203, v206
	v_mfma_f32_32x32x16_f16 v[34:49], v[2:5], v[150:153], 0
	v_mul_f32_e32 v67, v203, v209
	v_mul_f32_e32 v69, v203, v208
	v_mfma_f32_32x32x16_f16 v[34:49], v[18:21], v[146:149], v[34:49]
	v_fma_f32 v66, v202, v206, -v66
	v_fma_f32 v68, v202, v207, v68
	v_mfma_f32_32x32x16_f16 v[34:49], v[6:9], v[142:145], v[34:49]
	v_fma_f32 v67, v202, v208, -v67
	v_fma_f32 v69, v202, v209, v69
	v_mfma_f32_32x32x16_f16 v[34:49], v[22:25], v[138:141], v[34:49]
	v_cvt_pk_f16_f32 v218, v66, v67
	v_cvt_pk_f16_f32 v220, v68, v69
	s_waitcnt vmcnt(2)
	v_mul_f32_e32 v70, v205, v211
	v_mul_f32_e32 v72, v205, v210
	v_mfma_f32_32x32x16_f16 v[50:65], v[2:5], v[134:137], 0
	v_mul_f32_e32 v71, v205, v213
	v_mul_f32_e32 v73, v205, v212
	v_mfma_f32_32x32x16_f16 v[50:65], v[18:21], v[126:129], v[50:65]
	v_fma_f32 v70, v204, v210, -v70
	v_fma_f32 v72, v204, v211, v72
	v_mfma_f32_32x32x16_f16 v[50:65], v[6:9], v[122:125], v[50:65]
	v_fma_f32 v71, v204, v212, -v71
	v_fma_f32 v73, v204, v213, v73
	v_mfma_f32_32x32x16_f16 v[50:65], v[22:25], v[130:133], v[50:65]
	v_cvt_pk_f16_f32 v219, v70, v71
	v_cvt_pk_f16_f32 v221, v72, v73
	v_xor_b32_e32 v255, 16, v254
	ds_read2_b64 v[206:209], v255 offset0:0 offset1:16
	ds_read2_b64 v[210:213], v255 offset0:32 offset1:48
	v_mfma_f32_32x32x16_f16 v[2:17], v[190:193], v[214:217], 0
	v_mfma_f32_32x32x16_f16 v[18:33], v[194:197], v[218:221], 0
	v_cvt_pk_f16_f32 v34, v34, v35
	v_cvt_pk_f16_f32 v35, v36, v37
	v_cvt_pk_f16_f32 v36, v38, v39
	v_cvt_pk_f16_f32 v37, v40, v41
	v_cvt_pk_f16_f32 v38, v42, v43
	v_cvt_pk_f16_f32 v39, v44, v45
	v_cvt_pk_f16_f32 v40, v46, v47
	v_cvt_pk_f16_f32 v41, v48, v49
	v_cvt_pk_f16_f32 v50, v50, v51
	v_cvt_pk_f16_f32 v51, v52, v53
	v_cvt_pk_f16_f32 v52, v54, v55
	v_cvt_pk_f16_f32 v53, v56, v57
	v_cvt_pk_f16_f32 v54, v58, v59
	v_cvt_pk_f16_f32 v55, v60, v61
	v_cvt_pk_f16_f32 v56, v62, v63
	v_cvt_pk_f16_f32 v57, v64, v65
	s_waitcnt vmcnt(2)
	v_cvt_pk_f16_f32 v2, v2, v3
	v_cvt_pk_f16_f32 v3, v4, v5
	v_cvt_pk_f16_f32 v4, v6, v7
	v_cvt_pk_f16_f32 v5, v8, v9
	v_mfma_f32_32x32x16_f16 v[90:105], v[34:37], v[222:225], 0
	v_cvt_pk_f16_f32 v6, v10, v11
	v_cvt_pk_f16_f32 v7, v12, v13
	v_cvt_pk_f16_f32 v8, v14, v15
	v_cvt_pk_f16_f32 v9, v16, v17
	v_mfma_f32_32x32x16_f16 v[106:121], v[34:37], v[238:241], 0
	v_cvt_pk_f16_f32 v18, v18, v19
	v_cvt_pk_f16_f32 v19, v20, v21
	v_cvt_pk_f16_f32 v20, v22, v23
	v_cvt_pk_f16_f32 v21, v24, v25
	v_mfma_f32_32x32x16_f16 v[90:105], v[38:41], v[226:229], v[90:105]
	v_cvt_pk_f16_f32 v22, v26, v27
	v_cvt_pk_f16_f32 v23, v28, v29
	v_cvt_pk_f16_f32 v24, v30, v31
	v_cvt_pk_f16_f32 v25, v32, v33
	v_mfma_f32_32x32x16_f16 v[106:121], v[38:41], v[242:245], v[106:121]
	s_waitcnt lgkmcnt(0)
	v_mul_f32_e32 v66, v199, v207
	v_mul_f32_e32 v68, v199, v206
	v_mul_f32_e32 v67, v199, v209
	v_mfma_f32_32x32x16_f16 v[90:105], v[50:53], v[230:233], v[90:105]
	v_mul_f32_e32 v69, v199, v208
	v_fma_f32 v66, v198, v206, -v66
	v_fma_f32 v68, v198, v207, v68
	v_fma_f32 v67, v198, v208, -v67
	v_mfma_f32_32x32x16_f16 v[106:121], v[50:53], v[246:249], v[106:121]
	v_fma_f32 v69, v198, v209, v69
	v_cvt_pk_f16_f32 v214, v66, v67
	v_cvt_pk_f16_f32 v216, v68, v69
	v_mul_f32_e32 v70, v201, v211
	v_mfma_f32_32x32x16_f16 v[90:105], v[54:57], v[234:237], v[90:105]
	v_mul_f32_e32 v72, v201, v210
	v_mul_f32_e32 v71, v201, v213
	v_mul_f32_e32 v73, v201, v212
	v_fma_f32 v70, v200, v210, -v70
	v_mfma_f32_32x32x16_f16 v[106:121], v[54:57], v[250:253], v[106:121]
	v_fma_f32 v72, v200, v211, v72
	v_fma_f32 v71, v200, v212, -v71
	v_fma_f32 v73, v200, v213, v73
	v_cvt_pk_f16_f32 v215, v70, v71
	v_cvt_pk_f16_f32 v217, v72, v73
	v_mfma_f32_32x32x16_f16 v[34:49], v[2:5], v[150:153], 0
	v_mul_f32_e32 v66, v203, v207
	v_mul_f32_e32 v68, v203, v206
	v_mul_f32_e32 v67, v203, v209
	v_mul_f32_e32 v69, v203, v208
	v_fma_f32 v66, v202, v206, -v66
	v_mfma_f32_32x32x16_f16 v[34:49], v[18:21], v[146:149], v[34:49]
	v_fma_f32 v68, v202, v207, v68
	v_fma_f32 v67, v202, v208, -v67
	v_fma_f32 v69, v202, v209, v69
	v_cvt_pk_f16_f32 v218, v66, v67
	v_cvt_pk_f16_f32 v220, v68, v69
	v_mfma_f32_32x32x16_f16 v[34:49], v[6:9], v[142:145], v[34:49]
	v_mul_f32_e32 v70, v205, v211
	v_mul_f32_e32 v72, v205, v210
	v_mul_f32_e32 v71, v205, v213
	v_mul_f32_e32 v73, v205, v212
	v_fma_f32 v70, v204, v210, -v70
	v_mfma_f32_32x32x16_f16 v[34:49], v[22:25], v[138:141], v[34:49]
	v_fma_f32 v72, v204, v211, v72
	v_fma_f32 v71, v204, v212, -v71
	v_fma_f32 v73, v204, v213, v73
	v_cvt_pk_f16_f32 v219, v70, v71
	v_cvt_pk_f16_f32 v221, v72, v73
	v_mfma_f32_32x32x16_f16 v[50:65], v[2:5], v[134:137], 0
	v_cvt_pk_f16_f32 v90, v90, v91
	v_cvt_pk_f16_f32 v91, v92, v93
	v_cvt_pk_f16_f32 v92, v94, v95
	v_cvt_pk_f16_f32 v93, v96, v97
	v_cvt_pk_f16_f32 v94, v98, v99
	v_mfma_f32_32x32x16_f16 v[50:65], v[18:21], v[126:129], v[50:65]
	v_cvt_pk_f16_f32 v95, v100, v101
	v_cvt_pk_f16_f32 v96, v102, v103
	v_cvt_pk_f16_f32 v97, v104, v105
	v_cvt_pk_f16_f32 v106, v106, v107
	v_cvt_pk_f16_f32 v107, v108, v109
	v_mfma_f32_32x32x16_f16 v[50:65], v[6:9], v[122:125], v[50:65]
	v_cvt_pk_f16_f32 v108, v110, v111
	v_cvt_pk_f16_f32 v109, v112, v113
	v_cvt_pk_f16_f32 v110, v114, v115
	v_cvt_pk_f16_f32 v111, v116, v117
	v_cvt_pk_f16_f32 v112, v118, v119
	v_mfma_f32_32x32x16_f16 v[50:65], v[22:25], v[130:133], v[50:65]
	v_cvt_pk_f16_f32 v113, v120, v121
	ds_write_b128 v173, v[90:93]
	ds_write_b128 v172, v[94:97]
	ds_write_b128 v173, v[106:109] offset:32768
	ds_write_b128 v172, v[110:113] offset:32768
	v_xor_b32_e32 v255, 24, v254
	ds_read2_b64 v[206:209], v255 offset0:0 offset1:16
	ds_read2_b64 v[210:213], v255 offset0:32 offset1:48
	v_mfma_f32_32x32x16_f16 v[2:17], v[190:193], v[214:217], 0
	v_mfma_f32_32x32x16_f16 v[18:33], v[194:197], v[218:221], 0
	v_cvt_pk_f16_f32 v34, v34, v35
	v_cvt_pk_f16_f32 v35, v36, v37
	v_cvt_pk_f16_f32 v36, v38, v39
	v_cvt_pk_f16_f32 v37, v40, v41
	v_cvt_pk_f16_f32 v38, v42, v43
	v_cvt_pk_f16_f32 v39, v44, v45
	v_cvt_pk_f16_f32 v40, v46, v47
	v_cvt_pk_f16_f32 v41, v48, v49
	v_cvt_pk_f16_f32 v50, v50, v51
	v_cvt_pk_f16_f32 v51, v52, v53
	v_cvt_pk_f16_f32 v52, v54, v55
	v_cvt_pk_f16_f32 v53, v56, v57
	v_cvt_pk_f16_f32 v54, v58, v59
	v_cvt_pk_f16_f32 v55, v60, v61
	v_cvt_pk_f16_f32 v56, v62, v63
	v_cvt_pk_f16_f32 v57, v64, v65
	v_mfma_f32_32x32x16_f16 v[90:105], v[34:37], v[222:225], 0
	v_cvt_pk_f16_f32 v2, v2, v3
	v_cvt_pk_f16_f32 v3, v4, v5
	v_cvt_pk_f16_f32 v4, v6, v7
	v_cvt_pk_f16_f32 v5, v8, v9
	v_mfma_f32_32x32x16_f16 v[106:121], v[34:37], v[238:241], 0
	v_cvt_pk_f16_f32 v6, v10, v11
	v_cvt_pk_f16_f32 v7, v12, v13
	v_cvt_pk_f16_f32 v8, v14, v15
	v_cvt_pk_f16_f32 v9, v16, v17
	v_cvt_pk_f16_f32 v18, v18, v19
	v_mfma_f32_32x32x16_f16 v[90:105], v[38:41], v[226:229], v[90:105]
	v_cvt_pk_f16_f32 v19, v20, v21
	v_cvt_pk_f16_f32 v20, v22, v23
	v_cvt_pk_f16_f32 v21, v24, v25
	v_cvt_pk_f16_f32 v22, v26, v27
	v_mfma_f32_32x32x16_f16 v[106:121], v[38:41], v[242:245], v[106:121]
	v_cvt_pk_f16_f32 v23, v28, v29
	v_cvt_pk_f16_f32 v24, v30, v31
	v_cvt_pk_f16_f32 v25, v32, v33
	s_waitcnt lgkmcnt(0)
	v_mul_f32_e32 v66, v199, v207
	v_mfma_f32_32x32x16_f16 v[90:105], v[50:53], v[230:233], v[90:105]
	v_mul_f32_e32 v68, v199, v206
	v_mul_f32_e32 v67, v199, v209
	v_mul_f32_e32 v69, v199, v208
	v_fma_f32 v66, v198, v206, -v66
	v_fma_f32 v68, v198, v207, v68
	v_mfma_f32_32x32x16_f16 v[106:121], v[50:53], v[246:249], v[106:121]
	v_fma_f32 v67, v198, v208, -v67
	v_fma_f32 v69, v198, v209, v69
	v_cvt_pk_f16_f32 v214, v66, v67
	v_cvt_pk_f16_f32 v216, v68, v69
	v_mfma_f32_32x32x16_f16 v[90:105], v[54:57], v[234:237], v[90:105]
	v_mul_f32_e32 v70, v201, v211
	v_mul_f32_e32 v72, v201, v210
	v_mul_f32_e32 v71, v201, v213
	v_mul_f32_e32 v73, v201, v212
	v_fma_f32 v70, v200, v210, -v70
	v_mfma_f32_32x32x16_f16 v[106:121], v[54:57], v[250:253], v[106:121]
	v_fma_f32 v72, v200, v211, v72
	v_fma_f32 v71, v200, v212, -v71
	v_fma_f32 v73, v200, v213, v73
	v_cvt_pk_f16_f32 v215, v70, v71
	v_cvt_pk_f16_f32 v217, v72, v73
	v_mfma_f32_32x32x16_f16 v[34:49], v[2:5], v[150:153], 0
	v_mul_f32_e32 v66, v203, v207
	v_mul_f32_e32 v68, v203, v206
	v_mul_f32_e32 v67, v203, v209
	v_mul_f32_e32 v69, v203, v208
	v_fma_f32 v66, v202, v206, -v66
	v_mfma_f32_32x32x16_f16 v[34:49], v[18:21], v[146:149], v[34:49]
	v_fma_f32 v68, v202, v207, v68
	v_fma_f32 v67, v202, v208, -v67
	v_fma_f32 v69, v202, v209, v69
	v_cvt_pk_f16_f32 v218, v66, v67
	v_cvt_pk_f16_f32 v220, v68, v69
	v_mfma_f32_32x32x16_f16 v[34:49], v[6:9], v[142:145], v[34:49]
	v_mul_f32_e32 v70, v205, v211
	v_mul_f32_e32 v72, v205, v210
	v_mul_f32_e32 v71, v205, v213
	v_mul_f32_e32 v73, v205, v212
	v_fma_f32 v70, v204, v210, -v70
	v_mfma_f32_32x32x16_f16 v[34:49], v[22:25], v[138:141], v[34:49]
	v_fma_f32 v72, v204, v211, v72
	v_fma_f32 v71, v204, v212, -v71
	v_fma_f32 v73, v204, v213, v73
	v_cvt_pk_f16_f32 v219, v70, v71
	v_cvt_pk_f16_f32 v221, v72, v73
	v_cvt_pk_f16_f32 v90, v90, v91
	v_mfma_f32_32x32x16_f16 v[50:65], v[2:5], v[134:137], 0
	v_cvt_pk_f16_f32 v91, v92, v93
	v_cvt_pk_f16_f32 v92, v94, v95
	v_cvt_pk_f16_f32 v93, v96, v97
	v_cvt_pk_f16_f32 v94, v98, v99
	v_cvt_pk_f16_f32 v95, v100, v101
	v_mfma_f32_32x32x16_f16 v[50:65], v[18:21], v[126:129], v[50:65]
	v_cvt_pk_f16_f32 v96, v102, v103
	v_cvt_pk_f16_f32 v97, v104, v105
	v_cvt_pk_f16_f32 v106, v106, v107
	v_cvt_pk_f16_f32 v107, v108, v109
	v_cvt_pk_f16_f32 v108, v110, v111
	v_mfma_f32_32x32x16_f16 v[50:65], v[6:9], v[122:125], v[50:65]
	v_cvt_pk_f16_f32 v109, v112, v113
	v_cvt_pk_f16_f32 v110, v114, v115
	v_cvt_pk_f16_f32 v111, v116, v117
	v_cvt_pk_f16_f32 v112, v118, v119
	v_cvt_pk_f16_f32 v113, v120, v121
	v_mfma_f32_32x32x16_f16 v[50:65], v[22:25], v[130:133], v[50:65]
	v_xor_b32_e32 v74, 0x8a0, v173
	v_xor_b32_e32 v75, 0x8a0, v172
	ds_write_b128 v74, v[90:93]
	ds_write_b128 v75, v[94:97]
	ds_write_b128 v74, v[106:109] offset:32768
	ds_write_b128 v75, v[110:113] offset:32768
	s_nop 0
	v_mfma_f32_32x32x16_f16 v[2:17], v[190:193], v[214:217], 0
	v_mfma_f32_32x32x16_f16 v[18:33], v[194:197], v[218:221], 0
	v_cvt_pk_f16_f32 v34, v34, v35
	v_cvt_pk_f16_f32 v35, v36, v37
	v_cvt_pk_f16_f32 v36, v38, v39
	v_cvt_pk_f16_f32 v37, v40, v41
	v_cvt_pk_f16_f32 v38, v42, v43
	v_cvt_pk_f16_f32 v39, v44, v45
	v_cvt_pk_f16_f32 v40, v46, v47
	v_cvt_pk_f16_f32 v41, v48, v49
	v_cvt_pk_f16_f32 v50, v50, v51
	v_cvt_pk_f16_f32 v51, v52, v53
	v_cvt_pk_f16_f32 v52, v54, v55
	v_cvt_pk_f16_f32 v53, v56, v57
	v_cvt_pk_f16_f32 v54, v58, v59
	v_cvt_pk_f16_f32 v55, v60, v61
	v_cvt_pk_f16_f32 v56, v62, v63
	v_cvt_pk_f16_f32 v57, v64, v65
	v_mfma_f32_32x32x16_f16 v[90:105], v[34:37], v[222:225], 0
	v_cvt_pk_f16_f32 v2, v2, v3
	v_cvt_pk_f16_f32 v3, v4, v5
	v_mfma_f32_32x32x16_f16 v[106:121], v[34:37], v[238:241], 0
	v_cvt_pk_f16_f32 v4, v6, v7
	v_cvt_pk_f16_f32 v5, v8, v9
	v_mfma_f32_32x32x16_f16 v[90:105], v[38:41], v[226:229], v[90:105]
	v_cvt_pk_f16_f32 v6, v10, v11
	v_cvt_pk_f16_f32 v7, v12, v13
	v_mfma_f32_32x32x16_f16 v[106:121], v[38:41], v[242:245], v[106:121]
	v_cvt_pk_f16_f32 v8, v14, v15
	v_cvt_pk_f16_f32 v9, v16, v17
	v_mfma_f32_32x32x16_f16 v[90:105], v[50:53], v[230:233], v[90:105]
	v_cvt_pk_f16_f32 v18, v18, v19
	v_cvt_pk_f16_f32 v19, v20, v21
	v_mfma_f32_32x32x16_f16 v[106:121], v[50:53], v[246:249], v[106:121]
	v_cvt_pk_f16_f32 v20, v22, v23
	v_cvt_pk_f16_f32 v21, v24, v25
	v_mfma_f32_32x32x16_f16 v[90:105], v[54:57], v[234:237], v[90:105]
	v_cvt_pk_f16_f32 v22, v26, v27
	v_cvt_pk_f16_f32 v23, v28, v29
	v_mfma_f32_32x32x16_f16 v[106:121], v[54:57], v[250:253], v[106:121]
	v_cvt_pk_f16_f32 v24, v30, v31
	v_cvt_pk_f16_f32 v25, v32, v33
	v_mfma_f32_32x32x16_f16 v[34:49], v[2:5], v[150:153], 0
	v_mfma_f32_32x32x16_f16 v[34:49], v[18:21], v[146:149], v[34:49]
	v_mfma_f32_32x32x16_f16 v[34:49], v[6:9], v[142:145], v[34:49]
	v_mfma_f32_32x32x16_f16 v[34:49], v[22:25], v[138:141], v[34:49]
	v_mfma_f32_32x32x16_f16 v[50:65], v[2:5], v[134:137], 0
	s_nop 5
	v_cvt_pk_f16_f32 v90, v90, v91
	v_cvt_pk_f16_f32 v91, v92, v93
	v_cvt_pk_f16_f32 v92, v94, v95
	v_cvt_pk_f16_f32 v93, v96, v97
	v_mfma_f32_32x32x16_f16 v[50:65], v[18:21], v[126:129], v[50:65]
	v_cvt_pk_f16_f32 v94, v98, v99
	v_cvt_pk_f16_f32 v95, v100, v101
	v_cvt_pk_f16_f32 v96, v102, v103
	v_cvt_pk_f16_f32 v97, v104, v105
	v_cvt_pk_f16_f32 v106, v106, v107
	v_cvt_pk_f16_f32 v107, v108, v109
	v_mfma_f32_32x32x16_f16 v[50:65], v[6:9], v[122:125], v[50:65]
	v_cvt_pk_f16_f32 v108, v110, v111
	v_cvt_pk_f16_f32 v109, v112, v113
	v_cvt_pk_f16_f32 v110, v114, v115
	v_cvt_pk_f16_f32 v111, v116, v117
	v_cvt_pk_f16_f32 v112, v118, v119
	v_cvt_pk_f16_f32 v113, v120, v121
	v_mfma_f32_32x32x16_f16 v[50:65], v[22:25], v[130:133], v[50:65]
	v_xor_b32_e32 v74, 0x1040, v173
	v_xor_b32_e32 v75, 0x1040, v172
	ds_write_b128 v74, v[90:93]
	ds_write_b128 v75, v[94:97]
	ds_write_b128 v74, v[106:109] offset:32768
	ds_write_b128 v75, v[110:113] offset:32768
	s_nop 11
	v_cvt_pk_f16_f32 v34, v34, v35
	v_cvt_pk_f16_f32 v35, v36, v37
	v_cvt_pk_f16_f32 v36, v38, v39
	v_cvt_pk_f16_f32 v37, v40, v41
	v_cvt_pk_f16_f32 v38, v42, v43
	v_cvt_pk_f16_f32 v39, v44, v45
	v_cvt_pk_f16_f32 v40, v46, v47
	v_cvt_pk_f16_f32 v41, v48, v49
	v_cvt_pk_f16_f32 v50, v50, v51
	v_cvt_pk_f16_f32 v51, v52, v53
	v_cvt_pk_f16_f32 v52, v54, v55
	v_cvt_pk_f16_f32 v53, v56, v57
	v_cvt_pk_f16_f32 v54, v58, v59
	v_cvt_pk_f16_f32 v55, v60, v61
	v_cvt_pk_f16_f32 v56, v62, v63
	v_cvt_pk_f16_f32 v57, v64, v65
	v_mfma_f32_32x32x16_f16 v[90:105], v[34:37], v[222:225], 0
	v_mfma_f32_32x32x16_f16 v[106:121], v[34:37], v[238:241], 0
	v_mfma_f32_32x32x16_f16 v[90:105], v[38:41], v[226:229], v[90:105]
	v_mfma_f32_32x32x16_f16 v[106:121], v[38:41], v[242:245], v[106:121]
	v_mfma_f32_32x32x16_f16 v[90:105], v[50:53], v[230:233], v[90:105]
	v_mfma_f32_32x32x16_f16 v[106:121], v[50:53], v[246:249], v[106:121]
	v_mfma_f32_32x32x16_f16 v[90:105], v[54:57], v[234:237], v[90:105]
	v_mfma_f32_32x32x16_f16 v[106:121], v[54:57], v[250:253], v[106:121]
	v_and_b32_e32 v134, 1, v156
	v_bitop3_b32 v132, v171, s40, v170 bitop3:0x36
	v_bitop3_b32 v131, s41, v154, v160 bitop3:0x36
	v_bitop3_b32 v135, v171, s42, v170 bitop3:0x36
	v_xor_b32_e32 v133, s43, v154
	v_and_b32_e32 v130, 4, v156
	s_lshl_b32 s2, s27, 3
	s_lshl_b32 s3, s5, 2
	s_or_b32 s2, s3, s2
	s_ashr_i32 s3, s2, 31
	s_lshl_b64 s[2:3], s[2:3], 13
	s_add_u32 s2, s20, s2
	s_addc_u32 s3, s21, s3
	v_lshlrev_b32_e32 v154, 1, v169
	v_lshl_add_u64 v[2:3], s[2:3], 0, v[154:155]
	v_add_co_u32_e32 v2, vcc, s23, v2
	s_nop 1
	v_addc_co_u32_e32 v3, vcc, 0, v3, vcc
	v_cvt_pk_f16_f32 v90, v90, v91
	v_cvt_pk_f16_f32 v91, v92, v93
	v_cvt_pk_f16_f32 v92, v94, v95
	v_cvt_pk_f16_f32 v93, v96, v97
	v_cvt_pk_f16_f32 v94, v98, v99
	v_cvt_pk_f16_f32 v95, v100, v101
	v_cvt_pk_f16_f32 v96, v102, v103
	v_cvt_pk_f16_f32 v97, v104, v105
	v_cvt_pk_f16_f32 v106, v106, v107
	v_cvt_pk_f16_f32 v107, v108, v109
	v_cvt_pk_f16_f32 v108, v110, v111
	v_cvt_pk_f16_f32 v109, v112, v113
	v_cvt_pk_f16_f32 v110, v114, v115
	v_cvt_pk_f16_f32 v111, v116, v117
	v_cvt_pk_f16_f32 v112, v118, v119
	v_cvt_pk_f16_f32 v113, v120, v121
	v_xor_b32_e32 v74, 0x18e0, v173
	v_xor_b32_e32 v75, 0x18e0, v172
	ds_write_b128 v74, v[90:93]
	ds_write_b128 v75, v[94:97]
	ds_write_b128 v74, v[106:109] offset:32768
	ds_write_b128 v75, v[110:113] offset:32768
	s_setprio 0
	s_waitcnt lgkmcnt(0)
	s_barrier
	global_load_dwordx4 v[62:65], v154, s[2:3]
	global_load_dwordx4 v[46:49], v154, s[2:3] offset:1024
	global_load_dwordx4 v[42:45], v154, s[2:3] offset:2048
	global_load_dwordx4 v[38:41], v154, s[2:3] offset:3072
	global_load_dwordx4 v[54:57], v[2:3], off offset:1024
	global_load_dwordx4 v[50:53], v[2:3], off offset:2048
	v_lshl_add_u64 v[4:5], s[12:13], 0, v[154:155]
	global_load_dwordx4 v[126:129], v154, s[12:13]
	global_load_dwordx4 v[122:125], v154, s[12:13] offset:1024
	global_load_dwordx4 v[118:121], v154, s[12:13] offset:2048
	global_load_dwordx4 v[114:117], v154, s[12:13] offset:3072
	global_load_dwordx4 v[34:37], v168, s[2:3]
	global_load_dwordx4 v[110:113], v168, s[12:13]
	v_add_co_u32_e32 v4, vcc, s23, v4
	s_nop 1
	v_addc_co_u32_e32 v5, vcc, 0, v5, vcc
	global_load_dwordx4 v[58:61], v[2:3], off offset:3072
	global_load_dwordx4 v[106:109], v[4:5], off offset:1024
	global_load_dwordx4 v[94:97], v[4:5], off offset:2048
	global_load_dwordx4 v[90:93], v[4:5], off offset:3072
	v_bfrev_b32_e32 v3, v156
	v_lshlrev_b32_e32 v7, 5, v167
	v_lshlrev_b32_e32 v6, 9, v167
	v_and_b32_e32 v7, 0x200, v7
	v_lshlrev_b32_e32 v8, 8, v167
	v_lshrrev_b32_e32 v3, 27, v3
	v_lshrrev_b32_e32 v2, 2, v167
	v_lshrrev_b32_e32 v4, 4, v156
	v_xor_b32_e32 v5, v169, v156
	v_and_b32_e32 v6, 0x5800, v6
	v_and_b32_e32 v3, 8, v3
	v_and_or_b32 v7, v8, s24, v7
	v_lshrrev_b32_e32 v5, 1, v5
	v_xor_b32_e32 v4, v2, v4
	v_or3_b32 v3, v7, v6, v3
	v_bitop3_b32 v7, v2, v182, 1 bitop3:0x6c
	v_lshlrev_b32_e32 v2, 1, v167
	v_and_b32_e32 v5, 4, v5
	v_lshlrev_b32_e32 v4, 3, v4
	v_lshrrev_b32_e32 v6, 1, v167
	v_and_b32_e32 v2, 2, v2
	v_and_or_b32 v9, v169, 8, v2
	v_and_b32_e32 v2, 8, v4
	v_and_or_b32 v4, v6, 2, v5
	v_or3_b32 v2, v4, v2, v134
	v_lshlrev_b32_e32 v2, 4, v2
	v_bitop3_b32 v146, v3, s28, v2 bitop3:0x36
	v_xor_b32_e32 v8, v6, v182
	v_xor_b32_e32 v147, 0x2010, v146
	v_lshlrev_b32_e32 v8, 2, v8
	v_and_b32_e32 v8, 4, v8
	v_or3_b32 v6, v9, v7, v8
	v_lshlrev_b32_e32 v7, 11, v167
	v_and_b32_e32 v8, 0x7800, v7
	v_lshlrev_b32_e32 v6, 4, v6
	v_or3_b32 v22, v6, v8, v170
	v_and_b32_e32 v23, 0x8000, v7
	v_xor_b32_e32 v150, 16, v146
	v_xad_u32 v70, v22, s28, v23
	v_xor_b32_e32 v151, 0x2000, v146
	ds_read_b64_tr_b16 v[18:19], v146
	ds_read_b64_tr_b16 v[20:21], v147
	ds_read_b64_tr_b16 v[22:23], v146 offset:32768
	ds_read_b64_tr_b16 v[24:25], v147 offset:32768
	ds_read_b64_tr_b16 v[26:27], v150
	ds_read_b64_tr_b16 v[28:29], v151
	ds_read_b64_tr_b16 v[30:31], v150 offset:32768
	ds_read_b64_tr_b16 v[32:33], v151 offset:32768
	v_xor_b32_e32 v148, 32, v146
	v_xor_b32_e32 v149, 0x2030, v146
	v_xor_b32_e32 v144, 48, v146
	v_xor_b32_e32 v145, 0x2020, v146
	v_xor_b32_e32 v142, 64, v146
	v_xor_b32_e32 v143, 0x2050, v146
	v_xor_b32_e32 v140, 0x50, v146
	v_xor_b32_e32 v141, 0x2040, v146
	v_xor_b32_e32 v138, 0x60, v146
	v_xor_b32_e32 v139, 0x2070, v146
	v_xor_b32_e32 v136, 0x70, v146
	v_xor_b32_e32 v137, 0x2060, v146
	v_xor_b32_e32 v71, 0x60, v70
	s_lshl_b64 s[0:1], s[0:1], 13
	s_add_u32 s0, s8, s0
	s_addc_u32 s1, s9, s1
	s_waitcnt vmcnt(17) lgkmcnt(4)
	v_mfma_f32_32x32x16_f16 v[2:17], v[18:21], v[86:89], 0
	s_waitcnt vmcnt(16)
	v_mfma_f32_32x32x16_f16 v[2:17], v[22:25], v[82:85], v[2:17]
	ds_read_b64_tr_b16 v[206:207], v148
	ds_read_b64_tr_b16 v[208:209], v149
	ds_read_b64_tr_b16 v[210:211], v148 offset:32768
	ds_read_b64_tr_b16 v[212:213], v149 offset:32768
	s_waitcnt lgkmcnt(4)
	v_mfma_f32_32x32x16_f16 v[190:205], v[26:29], v[86:89], 0
	v_mfma_f32_32x32x16_f16 v[190:205], v[30:33], v[82:85], v[190:205]
	s_nop 4
	v_cvt_pk_f16_f32 v2, v2, v3
	v_cvt_pk_f16_f32 v3, v4, v5
	v_cvt_pk_f16_f32 v4, v6, v7
	v_cvt_pk_f16_f32 v5, v8, v9
	v_cvt_pk_f16_f32 v6, v10, v11
	v_cvt_pk_f16_f32 v7, v12, v13
	v_cvt_pk_f16_f32 v8, v14, v15
	v_cvt_pk_f16_f32 v9, v16, v17
	v_xor_b32_e32 v73, 0x280, v70
	ds_write_b128 v70, v[2:5]
	ds_write_b128 v73, v[6:9]
	ds_read_b64_tr_b16 v[18:19], v144
	ds_read_b64_tr_b16 v[20:21], v145
	ds_read_b64_tr_b16 v[22:23], v144 offset:32768
	ds_read_b64_tr_b16 v[24:25], v145 offset:32768
	s_waitcnt lgkmcnt(6)
	v_mfma_f32_32x32x16_f16 v[2:17], v[206:209], v[86:89], 0
	v_mfma_f32_32x32x16_f16 v[2:17], v[210:213], v[82:85], v[2:17]
	v_cvt_pk_f16_f32 v190, v190, v191
	v_cvt_pk_f16_f32 v191, v192, v193
	v_cvt_pk_f16_f32 v192, v194, v195
	v_cvt_pk_f16_f32 v193, v196, v197
	v_cvt_pk_f16_f32 v194, v198, v199
	v_cvt_pk_f16_f32 v195, v200, v201
	v_cvt_pk_f16_f32 v196, v202, v203
	v_cvt_pk_f16_f32 v197, v204, v205
	v_xor_b32_e32 v72, 16, v70
	v_xor_b32_e32 v73, 0x290, v70
	ds_write_b128 v72, v[190:193]
	ds_write_b128 v73, v[194:197]
	ds_read_b64_tr_b16 v[26:27], v142
	ds_read_b64_tr_b16 v[28:29], v143
	ds_read_b64_tr_b16 v[30:31], v142 offset:32768
	ds_read_b64_tr_b16 v[32:33], v143 offset:32768
	s_waitcnt lgkmcnt(6)
	v_mfma_f32_32x32x16_f16 v[190:205], v[18:21], v[86:89], 0
	v_mfma_f32_32x32x16_f16 v[190:205], v[22:25], v[82:85], v[190:205]
	v_cvt_pk_f16_f32 v2, v2, v3
	v_cvt_pk_f16_f32 v3, v4, v5
	v_cvt_pk_f16_f32 v4, v6, v7
	v_cvt_pk_f16_f32 v5, v8, v9
	v_cvt_pk_f16_f32 v6, v10, v11
	v_cvt_pk_f16_f32 v7, v12, v13
	v_cvt_pk_f16_f32 v8, v14, v15
	v_cvt_pk_f16_f32 v9, v16, v17
	v_xor_b32_e32 v72, 32, v70
	v_xor_b32_e32 v73, 0x2a0, v70
	ds_write_b128 v72, v[2:5]
	ds_write_b128 v73, v[6:9]
	ds_read_b64_tr_b16 v[206:207], v140
	ds_read_b64_tr_b16 v[208:209], v141
	ds_read_b64_tr_b16 v[210:211], v140 offset:32768
	ds_read_b64_tr_b16 v[212:213], v141 offset:32768
	s_waitcnt lgkmcnt(6)
	v_mfma_f32_32x32x16_f16 v[2:17], v[26:29], v[86:89], 0
	v_mfma_f32_32x32x16_f16 v[2:17], v[30:33], v[82:85], v[2:17]
	v_cvt_pk_f16_f32 v190, v190, v191
	v_cvt_pk_f16_f32 v191, v192, v193
	v_cvt_pk_f16_f32 v192, v194, v195
	v_cvt_pk_f16_f32 v193, v196, v197
	v_cvt_pk_f16_f32 v194, v198, v199
	v_cvt_pk_f16_f32 v195, v200, v201
	v_cvt_pk_f16_f32 v196, v202, v203
	v_cvt_pk_f16_f32 v197, v204, v205
	v_xor_b32_e32 v72, 48, v70
	v_xor_b32_e32 v73, 0x2b0, v70
	ds_write_b128 v72, v[190:193]
	ds_write_b128 v73, v[194:197]
	ds_read_b64_tr_b16 v[18:19], v138
	ds_read_b64_tr_b16 v[20:21], v139
	ds_read_b64_tr_b16 v[22:23], v138 offset:32768
	ds_read_b64_tr_b16 v[24:25], v139 offset:32768
	s_waitcnt lgkmcnt(6)
	v_mfma_f32_32x32x16_f16 v[190:205], v[206:209], v[86:89], 0
	v_mfma_f32_32x32x16_f16 v[190:205], v[210:213], v[82:85], v[190:205]
	v_cvt_pk_f16_f32 v2, v2, v3
	v_cvt_pk_f16_f32 v3, v4, v5
	v_cvt_pk_f16_f32 v4, v6, v7
	v_cvt_pk_f16_f32 v5, v8, v9
	v_cvt_pk_f16_f32 v6, v10, v11
	v_cvt_pk_f16_f32 v7, v12, v13
	v_cvt_pk_f16_f32 v8, v14, v15
	v_cvt_pk_f16_f32 v9, v16, v17
	v_xor_b32_e32 v72, 64, v70
	v_xor_b32_e32 v73, 0x2c0, v70
	ds_write_b128 v72, v[2:5]
	ds_write_b128 v73, v[6:9]
	ds_read_b64_tr_b16 v[26:27], v136
	ds_read_b64_tr_b16 v[28:29], v137
	ds_read_b64_tr_b16 v[30:31], v136 offset:32768
	ds_read_b64_tr_b16 v[32:33], v137 offset:32768
	s_waitcnt lgkmcnt(6)
	v_mfma_f32_32x32x16_f16 v[2:17], v[18:21], v[86:89], 0
	v_mfma_f32_32x32x16_f16 v[2:17], v[22:25], v[82:85], v[2:17]
	v_cvt_pk_f16_f32 v190, v190, v191
	v_cvt_pk_f16_f32 v191, v192, v193
	v_cvt_pk_f16_f32 v192, v194, v195
	v_cvt_pk_f16_f32 v193, v196, v197
	v_cvt_pk_f16_f32 v194, v198, v199
	v_cvt_pk_f16_f32 v195, v200, v201
	v_cvt_pk_f16_f32 v196, v202, v203
	v_cvt_pk_f16_f32 v197, v204, v205
	v_xor_b32_e32 v72, 0x50, v70
	v_xor_b32_e32 v73, 0x2d0, v70
	ds_write_b128 v72, v[190:193]
	ds_write_b128 v73, v[194:197]
	s_waitcnt lgkmcnt(2)
	v_mfma_f32_32x32x16_f16 v[190:205], v[26:29], v[86:89], 0
	v_mfma_f32_32x32x16_f16 v[190:205], v[30:33], v[82:85], v[190:205]
	v_cvt_pk_f16_f32 v2, v2, v3
	v_cvt_pk_f16_f32 v3, v4, v5
	v_cvt_pk_f16_f32 v4, v6, v7
	v_cvt_pk_f16_f32 v5, v8, v9
	v_cvt_pk_f16_f32 v6, v10, v11
	v_cvt_pk_f16_f32 v7, v12, v13
	v_cvt_pk_f16_f32 v8, v14, v15
	v_cvt_pk_f16_f32 v9, v16, v17
	v_xor_b32_e32 v72, 0x60, v70
	v_xor_b32_e32 v73, 0x2e0, v70
	ds_write_b128 v72, v[2:5]
	ds_write_b128 v73, v[6:9]
	v_cvt_pk_f16_f32 v190, v190, v191
	v_cvt_pk_f16_f32 v191, v192, v193
	v_cvt_pk_f16_f32 v192, v194, v195
	v_cvt_pk_f16_f32 v193, v196, v197
	v_cvt_pk_f16_f32 v194, v198, v199
	v_cvt_pk_f16_f32 v195, v200, v201
	v_cvt_pk_f16_f32 v196, v202, v203
	v_cvt_pk_f16_f32 v197, v204, v205
	v_xor_b32_e32 v72, 0x70, v70
	v_xor_b32_e32 v73, 0x2f0, v70
	ds_write_b128 v72, v[190:193]
	ds_write_b128 v73, v[194:197]
	v_lshl_add_u64 v[2:3], s[0:1], 0, v[154:155]
	v_lshl_add_u64 v[4:5], v[2:3], 0, s[18:19]
	v_add_co_u32_e32 v2, vcc, s25, v2
	s_waitcnt lgkmcnt(0)
	s_nop 0
	v_addc_co_u32_e32 v3, vcc, 0, v3, vcc
	s_barrier
	s_nop 0
	s_nop 0
	global_load_dwordx4 v[102:105], v[2:3], off
	global_load_dwordx4 v[98:101], v[4:5], off offset:1024
	s_setprio 1
	s_add_u32 s0, s2, 0x2000
	s_addc_u32 s1, s3, 0
	v_lshl_add_u64 v[2:3], s[0:1], 0, v[154:155]
	v_add_co_u32_e32 v2, vcc, s23, v2
	global_load_dwordx4 v[66:69], v154, s[0:1]
	global_load_dwordx4 v[70:73], v154, s[0:1] offset:1024
	global_load_dwordx4 v[74:77], v154, s[0:1] offset:2048
	global_load_dwordx4 v[78:81], v154, s[0:1] offset:3072
	v_addc_co_u32_e32 v3, vcc, 0, v3, vcc
	global_load_dwordx4 v[82:85], v168, s[0:1]
	global_load_dwordx4 v[86:89], v[2:3], off offset:1024
	global_load_dwordx4 v[182:185], v[2:3], off offset:2048
	global_load_dwordx4 v[186:189], v[2:3], off offset:3072
	ds_read_b128 v[18:21], v179
	ds_read_b128 v[22:25], v179 offset:32768
	ds_read_b128 v[26:29], v178
	ds_read_b128 v[30:33], v178 offset:32768
	s_add_u32 s0, s2, 0x6000
	s_addc_u32 s1, s3, 0
	s_waitcnt vmcnt(25) lgkmcnt(3)
	v_mfma_f32_32x32x16_f16 v[2:17], v[18:21], v[62:65], 0
	s_add_u32 s2, s2, 0x4000
	s_addc_u32 s3, s3, 0
	s_or_b32 s27, s26, 0x8a0
	s_or_b32 s26, s26, 0xa20
	s_waitcnt vmcnt(24) lgkmcnt(1)
	v_mfma_f32_32x32x16_f16 v[2:17], v[26:29], v[46:49], v[2:17]
	s_waitcnt vmcnt(23)
	v_mfma_f32_32x32x16_f16 v[2:17], v[22:25], v[42:45], v[2:17]
	s_waitcnt vmcnt(22) lgkmcnt(0)
	v_mfma_f32_32x32x16_f16 v[2:17], v[30:33], v[38:41], v[2:17]
	s_waitcnt vmcnt(15)
	v_mfma_f32_32x32x16_f16 v[34:49], v[18:21], v[34:37], 0
	s_nop 9
	v_cvt_pk_f16_f32 v9, v8, v9
	v_cvt_pk_f16_f32 v8, v6, v7
	v_cvt_pk_f16_f32 v7, v4, v5
	v_cvt_pk_f16_f32 v6, v2, v3
	v_cvt_pk_f16_f32 v5, v16, v17
	v_cvt_pk_f16_f32 v4, v14, v15
	v_cvt_pk_f16_f32 v3, v12, v13
	v_mfma_f32_32x32x16_f16 v[34:49], v[26:29], v[54:57], v[34:49]
	v_cvt_pk_f16_f32 v2, v10, v11
	v_mfma_f32_32x32x16_f16 v[34:49], v[22:25], v[50:53], v[34:49]
	s_waitcnt vmcnt(13)
	v_mfma_f32_32x32x16_f16 v[34:49], v[30:33], v[58:61], v[34:49]
	v_mfma_f32_32x32x16_f16 v[18:33], v[6:9], v[126:129], 0
	s_nop 10
	v_cvt_pk_f16_f32 v13, v40, v41
	v_cvt_pk_f16_f32 v12, v38, v39
	v_cvt_pk_f16_f32 v11, v36, v37
	v_cvt_pk_f16_f32 v10, v34, v35
	v_cvt_pk_f16_f32 v17, v48, v49
	v_cvt_pk_f16_f32 v16, v46, v47
	v_cvt_pk_f16_f32 v15, v44, v45
	v_mfma_f32_32x32x16_f16 v[50:65], v[6:9], v[110:113], 0
	v_bitop3_b32 v6, v171, s27, v170 bitop3:0x36
	v_cvt_pk_f16_f32 v14, v42, v43
	v_mfma_f32_32x32x16_f16 v[18:33], v[2:5], v[122:125], v[18:33]
	s_waitcnt vmcnt(12)
	v_mfma_f32_32x32x16_f16 v[50:65], v[2:5], v[106:109], v[50:65]
	ds_read_b128 v[2:5], v6
	ds_read_b128 v[6:9], v6 offset:32768
	v_mfma_f32_32x32x16_f16 v[18:33], v[10:13], v[118:121], v[18:33]
	s_waitcnt vmcnt(11)
	v_mfma_f32_32x32x16_f16 v[50:65], v[10:13], v[94:97], v[50:65]
	s_waitcnt vmcnt(7) lgkmcnt(1)
	v_mfma_f32_32x32x16_f16 v[34:49], v[2:5], v[66:69], 0
	v_mfma_f32_32x32x16_f16 v[18:33], v[14:17], v[114:117], v[18:33]
	v_mfma_f32_32x32x16_f16 v[50:65], v[14:17], v[90:93], v[50:65]
	v_bitop3_b32 v14, v171, s26, v170 bitop3:0x36
	ds_read_b128 v[10:13], v14
	ds_read_b128 v[14:17], v14 offset:32768
	s_nop 7
	v_cvt_pk_f16_f32 v25, v24, v25
	v_cvt_pk_f16_f32 v24, v22, v23
	v_cvt_pk_f16_f32 v23, v20, v21
	v_cvt_pk_f16_f32 v22, v18, v19
	v_cvt_pk_f16_f32 v21, v32, v33
	s_waitcnt vmcnt(6) lgkmcnt(1)
	v_mfma_f32_32x32x16_f16 v[34:49], v[10:13], v[70:73], v[34:49]
	v_cvt_pk_f16_f32 v20, v30, v31
	v_cvt_pk_f16_f32 v19, v28, v29
	v_cvt_pk_f16_f32 v18, v26, v27
	ds_write_b128 v173, v[22:25]
	ds_write_b128 v172, v[18:21]
	v_cvt_pk_f16_f32 v21, v56, v57
	v_cvt_pk_f16_f32 v20, v54, v55
	s_waitcnt vmcnt(5)
	v_mfma_f32_32x32x16_f16 v[34:49], v[6:9], v[74:77], v[34:49]
	v_cvt_pk_f16_f32 v19, v52, v53
	v_cvt_pk_f16_f32 v18, v50, v51
	ds_write_b128 v173, v[18:21] offset:32768
	v_cvt_pk_f16_f32 v21, v64, v65
	v_cvt_pk_f16_f32 v20, v62, v63
	v_cvt_pk_f16_f32 v19, v60, v61
	v_cvt_pk_f16_f32 v18, v58, v59
	s_waitcnt vmcnt(4) lgkmcnt(3)
	v_mfma_f32_32x32x16_f16 v[34:49], v[14:17], v[78:81], v[34:49]
	ds_write_b128 v172, v[18:21] offset:32768
	s_waitcnt vmcnt(3)
	v_mfma_f32_32x32x16_f16 v[66:81], v[2:5], v[82:85], 0
	s_nop 8
	v_cvt_pk_f16_f32 v41, v40, v41
	v_cvt_pk_f16_f32 v40, v38, v39
	v_cvt_pk_f16_f32 v39, v36, v37
	v_cvt_pk_f16_f32 v38, v34, v35
	v_cvt_pk_f16_f32 v85, v48, v49
	v_cvt_pk_f16_f32 v84, v46, v47
	v_cvt_pk_f16_f32 v83, v44, v45
	s_waitcnt vmcnt(2)
	v_mfma_f32_32x32x16_f16 v[66:81], v[10:13], v[86:89], v[66:81]
	v_cvt_pk_f16_f32 v82, v42, v43
	s_waitcnt vmcnt(1)
	v_mfma_f32_32x32x16_f16 v[66:81], v[6:9], v[182:185], v[66:81]
	s_waitcnt vmcnt(0)
	v_mfma_f32_32x32x16_f16 v[66:81], v[14:17], v[186:189], v[66:81]
	v_mfma_f32_32x32x16_f16 v[2:17], v[38:41], v[126:129], 0
	s_nop 10
	v_cvt_pk_f16_f32 v73, v72, v73
	v_cvt_pk_f16_f32 v72, v70, v71
	v_cvt_pk_f16_f32 v70, v66, v67
	v_cvt_pk_f16_f32 v67, v76, v77
	v_cvt_pk_f16_f32 v66, v74, v75
	global_load_dwordx4 v[74:77], v154, s[2:3]
	v_cvt_pk_f16_f32 v71, v68, v69
	v_cvt_pk_f16_f32 v69, v80, v81
	v_cvt_pk_f16_f32 v68, v78, v79
	global_load_dwordx4 v[78:81], v154, s[2:3] offset:1024
	ds_read_b128 v[18:21], v180
	ds_read_b128 v[22:25], v176
	ds_read_b128 v[26:29], v180 offset:32768
	global_load_dwordx4 v[30:33], v154, s[2:3] offset:2048
	v_mfma_f32_32x32x16_f16 v[34:49], v[38:41], v[110:113], 0
	v_mfma_f32_32x32x16_f16 v[2:17], v[82:85], v[122:125], v[2:17]
	v_mfma_f32_32x32x16_f16 v[34:49], v[82:85], v[106:109], v[34:49]
	ds_read_b128 v[82:85], v176 offset:32768
	s_waitcnt vmcnt(2) lgkmcnt(3)
	v_mfma_f32_32x32x16_f16 v[50:65], v[18:21], v[74:77], 0
	v_mfma_f32_32x32x16_f16 v[2:17], v[70:73], v[118:121], v[2:17]
	v_mfma_f32_32x32x16_f16 v[34:49], v[70:73], v[94:97], v[34:49]
	v_lshl_add_u64 v[70:71], s[2:3], 0, v[154:155]
	v_add_co_u32_e32 v152, vcc, s23, v70
	s_nop 1
	v_addc_co_u32_e32 v153, vcc, 0, v71, vcc
	s_waitcnt vmcnt(1) lgkmcnt(2)
	v_mfma_f32_32x32x16_f16 v[50:65], v[22:25], v[78:81], v[50:65]
	v_mfma_f32_32x32x16_f16 v[2:17], v[66:69], v[114:117], v[2:17]
	v_mfma_f32_32x32x16_f16 v[34:49], v[66:69], v[90:93], v[34:49]
	global_load_dwordx4 v[66:69], v154, s[2:3] offset:3072
	s_nop 9
	v_cvt_pk_f16_f32 v9, v8, v9
	v_cvt_pk_f16_f32 v8, v6, v7
	v_cvt_pk_f16_f32 v7, v4, v5
	v_cvt_pk_f16_f32 v6, v2, v3
	v_cvt_pk_f16_f32 v5, v16, v17
	v_cvt_pk_f16_f32 v4, v14, v15
	s_waitcnt vmcnt(1) lgkmcnt(1)
	v_mfma_f32_32x32x16_f16 v[50:65], v[26:29], v[30:33], v[50:65]
	global_load_dwordx4 v[30:33], v168, s[2:3]
	global_load_dwordx4 v[86:89], v[152:153], off offset:1024
	s_nop 0
	global_load_dwordx4 v[168:171], v168, s[0:1]
	v_cvt_pk_f16_f32 v3, v12, v13
	v_cvt_pk_f16_f32 v2, v10, v11
	ds_write_b128 v175, v[6:9]
	ds_write_b128 v174, v[2:5]
	v_cvt_pk_f16_f32 v5, v40, v41
	s_waitcnt vmcnt(3) lgkmcnt(2)
	v_mfma_f32_32x32x16_f16 v[50:65], v[82:85], v[66:69], v[50:65]
	global_load_dwordx4 v[182:185], v154, s[0:1] offset:1024
	v_cvt_pk_f16_f32 v4, v38, v39
	v_cvt_pk_f16_f32 v3, v36, v37
	v_cvt_pk_f16_f32 v2, v34, v35
	ds_write_b128 v175, v[2:5] offset:32768
	v_cvt_pk_f16_f32 v5, v48, v49
	v_cvt_pk_f16_f32 v4, v46, v47
	s_waitcnt vmcnt(3)
	v_mfma_f32_32x32x16_f16 v[66:81], v[18:21], v[30:33], 0
	global_load_dwordx4 v[18:21], v[152:153], off offset:2048
	v_cvt_pk_f16_f32 v3, v44, v45
	v_cvt_pk_f16_f32 v2, v42, v43
	ds_write_b128 v174, v[2:5] offset:32768
	v_cvt_pk_f16_f32 v57, v56, v57
	v_cvt_pk_f16_f32 v56, v54, v55
	v_cvt_pk_f16_f32 v55, v52, v53
	s_waitcnt vmcnt(3)
	v_mfma_f32_32x32x16_f16 v[66:81], v[22:25], v[86:89], v[66:81]
	global_load_dwordx4 v[22:25], v[152:153], off offset:3072
	v_cvt_pk_f16_f32 v54, v50, v51
	s_waitcnt vmcnt(1)
	v_mfma_f32_32x32x16_f16 v[66:81], v[26:29], v[18:21], v[66:81]
	v_lshl_add_u64 v[18:19], s[0:1], 0, v[154:155]
	v_add_co_u32_e32 v152, vcc, s23, v18
	s_nop 1
	v_addc_co_u32_e32 v153, vcc, 0, v19, vcc
	global_load_dwordx4 v[86:89], v[152:153], off offset:1024
	s_waitcnt vmcnt(1)
	v_mfma_f32_32x32x16_f16 v[66:81], v[82:85], v[22:25], v[66:81]
	v_cvt_pk_f16_f32 v85, v64, v65
	v_cvt_pk_f16_f32 v84, v62, v63
	v_cvt_pk_f16_f32 v83, v60, v61
	v_cvt_pk_f16_f32 v82, v58, v59
	v_mfma_f32_32x32x16_f16 v[18:33], v[54:57], v[126:129], 0
	s_nop 6
	v_cvt_pk_f16_f32 v73, v72, v73
	v_cvt_pk_f16_f32 v72, v70, v71
	v_cvt_pk_f16_f32 v70, v66, v67
	v_cvt_pk_f16_f32 v67, v76, v77
	v_cvt_pk_f16_f32 v66, v74, v75
	global_load_dwordx4 v[74:77], v154, s[0:1]
	ds_read_b128 v[2:5], v181
	ds_read_b128 v[6:9], v177
	ds_read_b128 v[10:13], v181 offset:32768
	global_load_dwordx4 v[14:17], v154, s[0:1] offset:2048
	global_load_dwordx4 v[34:37], v154, s[0:1] offset:3072
	v_mfma_f32_32x32x16_f16 v[50:65], v[54:57], v[110:113], 0
	v_cvt_pk_f16_f32 v71, v68, v69
	v_cvt_pk_f16_f32 v69, v80, v81
	v_cvt_pk_f16_f32 v68, v78, v79
	v_mfma_f32_32x32x16_f16 v[18:33], v[82:85], v[122:125], v[18:33]
	v_mfma_f32_32x32x16_f16 v[50:65], v[82:85], v[106:109], v[50:65]
	ds_read_b128 v[82:85], v177 offset:32768
	v_mfma_f32_32x32x16_f16 v[18:33], v[70:73], v[118:121], v[18:33]
	v_mfma_f32_32x32x16_f16 v[50:65], v[70:73], v[94:97], v[50:65]
	v_mfma_f32_32x32x16_f16 v[18:33], v[66:69], v[114:117], v[18:33]
	v_mfma_f32_32x32x16_f16 v[50:65], v[66:69], v[90:93], v[50:65]
	s_nop 10
	v_cvt_pk_f16_f32 v25, v24, v25
	v_cvt_pk_f16_f32 v24, v22, v23
	v_cvt_pk_f16_f32 v23, v20, v21
	v_cvt_pk_f16_f32 v22, v18, v19
	ds_write_b128 v132, v[22:25]
	s_waitcnt vmcnt(2) lgkmcnt(4)
	v_mfma_f32_32x32x16_f16 v[66:81], v[2:5], v[74:77], 0
	s_waitcnt lgkmcnt(3)
	v_mfma_f32_32x32x16_f16 v[66:81], v[6:9], v[182:185], v[66:81]
	s_waitcnt vmcnt(1) lgkmcnt(2)
	v_mfma_f32_32x32x16_f16 v[66:81], v[10:13], v[14:17], v[66:81]
	s_waitcnt vmcnt(0) lgkmcnt(1)
	v_mfma_f32_32x32x16_f16 v[66:81], v[82:85], v[34:37], v[66:81]
	v_mfma_f32_32x32x16_f16 v[34:49], v[2:5], v[168:171], 0
	global_load_dwordx4 v[2:5], v[152:153], off offset:2048
	s_nop 9
	v_cvt_pk_f16_f32 v73, v72, v73
	v_cvt_pk_f16_f32 v72, v70, v71
	v_cvt_pk_f16_f32 v71, v68, v69
	v_cvt_pk_f16_f32 v70, v66, v67
	v_cvt_pk_f16_f32 v69, v80, v81
	v_cvt_pk_f16_f32 v68, v78, v79
	v_mfma_f32_32x32x16_f16 v[34:49], v[6:9], v[86:89], v[34:49]
	global_load_dwordx4 v[6:9], v[152:153], off offset:3072
	v_cvt_pk_f16_f32 v67, v76, v77
	v_cvt_pk_f16_f32 v66, v74, v75
	s_waitcnt vmcnt(1)
	v_mfma_f32_32x32x16_f16 v[34:49], v[10:13], v[2:5], v[34:49]
	s_waitcnt vmcnt(0)
	v_mfma_f32_32x32x16_f16 v[34:49], v[82:85], v[6:9], v[34:49]
	v_mfma_f32_32x32x16_f16 v[2:17], v[70:73], v[126:129], 0
	s_nop 10
	v_cvt_pk_f16_f32 v41, v40, v41
	v_cvt_pk_f16_f32 v40, v38, v39
	v_cvt_pk_f16_f32 v38, v34, v35
	v_cvt_pk_f16_f32 v35, v44, v45
	v_cvt_pk_f16_f32 v34, v42, v43
	v_cvt_pk_f16_f32 v45, v32, v33
	v_cvt_pk_f16_f32 v44, v30, v31
	v_cvt_pk_f16_f32 v43, v28, v29
	v_cvt_pk_f16_f32 v42, v26, v27
	v_mfma_f32_32x32x16_f16 v[18:33], v[70:73], v[110:113], 0
	v_cvt_pk_f16_f32 v39, v36, v37
	v_cvt_pk_f16_f32 v37, v48, v49
	v_cvt_pk_f16_f32 v36, v46, v47
	ds_write_b128 v131, v[42:45]
	v_cvt_pk_f16_f32 v45, v56, v57
	v_cvt_pk_f16_f32 v44, v54, v55
	v_cvt_pk_f16_f32 v43, v52, v53
	v_mfma_f32_32x32x16_f16 v[2:17], v[66:69], v[122:125], v[2:17]
	v_cvt_pk_f16_f32 v42, v50, v51
	ds_write_b128 v132, v[42:45] offset:32768
	v_cvt_pk_f16_f32 v45, v64, v65
	v_cvt_pk_f16_f32 v44, v62, v63
	v_cvt_pk_f16_f32 v43, v60, v61
	v_cvt_pk_f16_f32 v42, v58, v59
	ds_write_b128 v131, v[42:45] offset:32768
	v_mfma_f32_32x32x16_f16 v[18:33], v[66:69], v[106:109], v[18:33]
	v_mfma_f32_32x32x16_f16 v[2:17], v[38:41], v[118:121], v[2:17]
	v_mfma_f32_32x32x16_f16 v[18:33], v[38:41], v[94:97], v[18:33]
	v_mfma_f32_32x32x16_f16 v[2:17], v[34:37], v[114:117], v[2:17]
	v_mfma_f32_32x32x16_f16 v[18:33], v[34:37], v[90:93], v[18:33]
	s_nop 10
	v_cvt_pk_f16_f32 v9, v8, v9
	v_cvt_pk_f16_f32 v8, v6, v7
	v_cvt_pk_f16_f32 v7, v4, v5
	v_cvt_pk_f16_f32 v6, v2, v3
	v_cvt_pk_f16_f32 v5, v16, v17
	v_cvt_pk_f16_f32 v4, v14, v15
	v_cvt_pk_f16_f32 v3, v12, v13
	v_cvt_pk_f16_f32 v2, v10, v11
	ds_write_b128 v135, v[6:9]
	ds_write_b128 v133, v[2:5]
	v_cvt_pk_f16_f32 v5, v24, v25
	v_cvt_pk_f16_f32 v4, v22, v23
	v_cvt_pk_f16_f32 v3, v20, v21
	v_cvt_pk_f16_f32 v2, v18, v19
	ds_write_b128 v135, v[2:5] offset:32768
	v_cvt_pk_f16_f32 v5, v32, v33
	v_cvt_pk_f16_f32 v4, v30, v31
	v_cvt_pk_f16_f32 v3, v28, v29
	v_cvt_pk_f16_f32 v2, v26, v27
	ds_write_b128 v133, v[2:5] offset:32768
	s_setprio 0
	s_waitcnt lgkmcnt(0)
	s_barrier
	s_cmp_lt_i32 s22, 0
	s_cbranch_scc0 .Lno_pref
	s_add_u32 s36, s10, 0x140000
	s_addc_u32 s37, s11, 0
	v_lshlrev_b32_e32 v192, 3, v156
	v_lshlrev_b32_e32 v193, 3, v167
	global_load_dwordx2 v[190:191], v192, s[36:37]
	global_load_dwordx2 v[194:195], v193, s[36:37] offset:2048
